# RWKV chunk loop: Gram/T-inverse stage LDS reads hoisted to the stage head; RHS-stage operands prefetched before the preceding wave-group barrier
# baseline (speedup 1.0000x reference)
; #define LAS __attribute__((address_space(3)))
; __device__ __forceinline__ unsigned long long pack4bf(f32x4 v) { return (unsigned long long)pk2(v[0], v[1]) | ((unsigned long long)pk2(v[2], v[3]) << 32); }
; #define MFMA32(a_, b_, c_) __builtin_amdgcn_mfma_f32_32x32x16_bf16((a_), (b_), (c_), 0, 0, 0)
; __device__ __forceinline__ void rwkv_chunk_unit(Frame& F, int unit, LAS unsigned char* regB, LAS unsigned* bcnt, unsigned& btarget) {
;     ...
;         { const int t = 16 * mi + fr, jb = 16 * nj + 4 * fq;
;           f32x4 g2 = (f32x4){0.f, 0.f, 0.f, 0.f}, g3 = g2, g4 = g2;
; #pragma unroll
;           for (int ks = 0; ks < 2; ++ks) { const s16x8 bj = *(const LAS s16x8*)(Bt + (16 * nj + fr) * KS + 32 * ks + 8 * fq), kj = *(const LAS s16x8*)(Kt + (16 * nj + fr) * KS + 32 * ks + 8 * fq);
;               const s16x8 at = *(const LAS s16x8*)(At + (16 * mi + fr) * KS + 32 * ks + 8 * fq), rt = *(const LAS s16x8*)(Rt + (16 * mi + fr) * KS + 32 * ks + 8 * fq);
;               g2 = __builtin_amdgcn_mfma_f32_16x16x32_bf16(kj, at, g2, 0, 0, 0); g3 = __builtin_amdgcn_mfma_f32_16x16x32_bf16(bj, rt, g3, 0, 0, 0); g4 = __builtin_amdgcn_mfma_f32_16x16x32_bf16(kj, rt, g4, 0, 0, 0); }
; #pragma unroll
;           for (int rg_ = 0; rg_ < 4; ++rg_) { const int j = jb + rg_; g2[rg_] = (j < t) ? g2[rg_] : 0.f; g3[rg_] = (j <= t) ? g3[rg_] : 0.f; g4[rg_] = (j <= t) ? g4[rg_] : 0.f; }
;           *(LAS unsigned long long*)(G2b + t * LS + jb) = pack4bf(g2); *(LAS unsigned long long*)(G3b + t * LS + jb) = pack4bf(g3); *(LAS unsigned long long*)(G4b + t * LS + jb) = pack4bf(g4); }
;         { const int tq = lane & 31, hq = lane >> 5;
;           f32x16 Pm, Qm, Aq;
; #pragma unroll
;           for (int i = 0; i < 16; ++i) { Pm[i] = 0.f; Qm[i] = 0.f; }
; #pragma unroll
;           for (int s = 0; s < 4; ++s) { const s16x8 fa = *(const LAS s16x8*)(At + tq * KS + 16 * s + 8 * hq), fb = *(const LAS s16x8*)(Bt + tq * KS + 16 * s + 8 * hq);
;               Pm = MFMA32(fa, fb, Pm); Qm = MFMA32(fb, fa, Qm); }
; #pragma unroll
;           for (int i = 0; i < 16; ++i) { const int r_ = (i & 3) + 8 * (i >> 2) + 4 * hq;
;               Pm[i] = (tq < r_) ? Pm[i] : 0.f;
;               Qm[i] = (r_ < tq) ? Qm[i] : 0.f;
;               Aq[i] = Qm[i] + ((r_ == tq) ? 1.f : 0.f); }
.LBB0_1021:
	ds_read_b128 v[2:5], v105 offset:4608
	ds_read_b128 v[6:9], v105 offset:9216
	ds_read_b128 v[10:13], v168
	ds_read_b128 v[14:17], v168 offset:13824
	ds_read_b128 v[212:215], v105 offset:4672
	ds_read_b128 v[18:21], v105 offset:9280
	ds_read_b128 v[22:25], v168 offset:64
	ds_read_b128 v[26:29], v168 offset:13888
	ds_read_b128 v[216:219], v170 offset:4608
	ds_read_b128 v[220:223], v170
	ds_read_b128 v[224:227], v170 offset:32
	ds_read_b128 v[228:231], v170 offset:4640
	ds_read_b128 v[232:235], v170 offset:64
	ds_read_b128 v[244:247], v170 offset:4672
	v_readlane_b32 s4, v236, 35
	v_readlane_b32 s5, v236, 36
	s_and_b64 vcc, exec, s[2:3]
	s_waitcnt lgkmcnt(11)
	v_mfma_f32_16x16x32_bf16 v[10:13], v[6:9], v[10:13], 0
	s_waitcnt lgkmcnt(10)
	v_mfma_f32_16x16x32_bf16 v[2:5], v[2:5], v[14:17], 0
	v_mfma_f32_16x16x32_bf16 v[6:9], v[6:9], v[14:17], 0
	s_waitcnt lgkmcnt(7)
	v_mfma_f32_16x16x32_bf16 v[10:13], v[18:21], v[22:25], v[10:13]
	s_waitcnt lgkmcnt(6)
	v_mfma_f32_16x16x32_bf16 v[2:5], v[212:215], v[26:29], v[2:5]
	s_nop 5
	v_cndmask_b32_e64 v10, 0, v10, s[14:15]
	v_mfma_f32_16x16x32_bf16 v[6:9], v[18:21], v[26:29], v[6:9]
	v_cndmask_b32_e64 v14, v2, 0, s[16:17]
	v_cndmask_b32_e64 v2, 0, v11, s[4:5]
	v_readlane_b32 s4, v236, 37
	v_readlane_b32 s5, v236, 38
	v_cndmask_b32_e64 v11, 0, v3, s[14:15]
	v_cndmask_b32_e64 v5, v5, 0, s[26:27]
	v_cndmask_b32_e64 v3, 0, v12, s[4:5]
	v_readlane_b32 s4, v236, 39
	v_readlane_b32 s5, v236, 40
	v_cndmask_b32_e64 v12, v4, 0, s[22:23]
	v_cndmask_b32_e64 v6, v6, 0, s[16:17]
	v_cndmask_b32_e64 v4, 0, v13, s[4:5]
	v_cndmask_b32_e64 v7, 0, v7, s[14:15]
	v_cndmask_b32_e64 v8, v8, 0, s[22:23]
	v_cndmask_b32_e64 v9, v9, 0, s[26:27]
	v_cvt_pk_bf16_f32 v2, v10, v2
	v_cvt_pk_bf16_f32 v3, v3, v4
	v_cvt_pk_bf16_f32 v4, v14, v11
	v_cvt_pk_bf16_f32 v5, v12, v5
	ds_write2st64_b64 v169, v[2:3], v[4:5] offset0:50 offset1:55
	v_cvt_pk_bf16_f32 v2, v6, v7
	v_cvt_pk_bf16_f32 v3, v8, v9
	ds_write_b64 v169, v[2:3] offset:30720
	ds_read_b128 v[34:37], v170 offset:96
	ds_read_b128 v[38:41], v170 offset:4704
	s_waitcnt lgkmcnt(2)
	v_mfma_f32_32x32x16_bf16 v[18:33], v[220:223], v[216:219], 0
	v_readlane_b32 s4, v236, 41
	v_readlane_b32 s5, v236, 42
	v_mfma_f32_32x32x16_bf16 v[2:17], v[216:219], v[220:223], 0
	v_mfma_f32_32x32x16_bf16 v[18:33], v[224:227], v[228:231], v[18:33]
	v_mfma_f32_32x32x16_bf16 v[2:17], v[228:231], v[224:227], v[2:17]
	v_mfma_f32_32x32x16_bf16 v[18:33], v[232:235], v[244:247], v[18:33]
	v_mfma_f32_32x32x16_bf16 v[2:17], v[244:247], v[232:235], v[2:17]
	s_waitcnt lgkmcnt(0)
	v_mfma_f32_32x32x16_bf16 v[18:33], v[34:37], v[38:41], v[18:33]
	v_mfma_f32_32x32x16_bf16 v[2:17], v[38:41], v[34:37], v[2:17]
	s_nop 10
	v_cndmask_b32_e64 v18, 0, v18, s[4:5]
	v_readlane_b32 s4, v236, 43
	v_readlane_b32 s5, v236, 44
	v_cndmask_b32_e64 v19, v19, 0, s[30:31]
	v_cndmask_b32_e64 v21, 0, v21, s[24:25]
	v_cndmask_b32_e64 v24, 0, v24, s[52:53]
	v_cndmask_b32_e64 v25, 0, v25, s[54:55]
	v_cndmask_b32_e64 v41, 0, v3, s[4:5]
	v_readlane_b32 s4, v236, 45
	v_readlane_b32 s5, v236, 46
	v_cndmask_b32_e64 v40, 0, v2, s[30:31]
	v_cndmask_b32_e64 v35, 0, v5, s[28:29]
	v_cndmask_b32_e64 v20, 0, v20, s[4:5]
	v_readlane_b32 s4, v236, 47
	v_readlane_b32 s5, v236, 48
	v_cndmask_b32_e64 v34, 0, v4, s[34:35]
	v_cndmask_b32_e64 v39, 0, v9, s[56:57]
	v_cndmask_b32_e64 v22, 0, v22, s[4:5]
	v_readlane_b32 s4, v236, 49
	v_readlane_b32 s5, v236, 50
	v_cndmask_b32_e64 v38, 0, v8, s[58:59]
	v_cvt_pk_bf16_f32 v18, v18, v19
	v_cndmask_b32_e64 v23, 0, v23, s[4:5]
	v_readlane_b32 s4, v236, 51
	v_readlane_b32 s5, v236, 52
	v_cvt_pk_bf16_f32 v19, v20, v21
	v_cvt_pk_bf16_f32 v20, v22, v23
	v_cndmask_b32_e64 v37, 0, v7, s[4:5]
	v_readlane_b32 s4, v236, 53
	v_readlane_b32 s5, v236, 54
	v_cvt_pk_bf16_f32 v21, v24, v25
	v_cvt_pk_bf16_f32 v22, v40, v41
	v_cndmask_b32_e64 v36, 0, v6, s[4:5]
	v_cvt_pk_bf16_f32 v23, v34, v35
	v_cvt_pk_bf16_f32 v24, v36, v37
	v_cvt_pk_bf16_f32 v25, v38, v39
	v_cndmask_b32_e64 v42, 0, v26, s[60:61]
	v_cndmask_b32_e64 v43, 0, v27, s[62:63]
	v_cndmask_b32_e64 v44, 0, v28, s[68:69]
	v_cndmask_b32_e64 v45, 0, v29, s[70:71]
	v_cndmask_b32_e64 v46, 0, v30, s[76:77]
	v_cndmask_b32_e64 v47, 0, v31, s[78:79]
	v_cndmask_b32_e64 v48, 0, v32, s[84:85]
	v_cndmask_b32_e64 v49, 0, v33, s[86:87]
	v_add_f32_e32 v2, v185, v40
	v_add_f32_e32 v3, v186, v41
	v_pk_add_f32 v[4:5], v[106:107], v[34:35]
	v_pk_add_f32 v[6:7], v[108:109], v[36:37]
	v_pk_add_f32 v[8:9], v[110:111], v[38:39]
	v_cvt_pk_bf16_f32 v200, v42, v43
	v_cvt_pk_bf16_f32 v201, v44, v45
	v_cvt_pk_bf16_f32 v202, v46, v47
	v_cvt_pk_bf16_f32 v203, v48, v49
	v_mfma_f32_32x32x16_bf16 v[34:49], v[22:25], v[18:21], 0
	v_cndmask_b32_e64 v27, 0, v11, s[64:65]
	v_cndmask_b32_e64 v26, 0, v10, s[66:67]
	v_cndmask_b32_e64 v29, 0, v13, s[72:73]
	v_cndmask_b32_e64 v28, 0, v12, s[74:75]
	v_cndmask_b32_e64 v31, 0, v15, s[80:81]
; __device__ __forceinline__ s16x8 accfrag(const f32x16& x, int s) { v4u p; p.x = pk2(x[8 * s], x[8 * s + 1]); p.y = pk2(x[8 * s + 2], x[8 * s + 3]); p.z = pk2(x[8 * s + 4], x[8 * s + 5]); p.w = pk2(x[8 * s + 6], x[8 * s + 7]); return __builtin_bit_cast(s16x8, p); }
; #define MFMA32(a_, b_, c_) __builtin_amdgcn_mfma_f32_32x32x16_bf16((a_), (b_), (c_), 0, 0, 0)
; __device__ __forceinline__ void rwkv_chunk_unit(Frame& F, int unit, LAS unsigned char* regB, LAS unsigned* bcnt, unsigned& btarget) {
;     ...
; #pragma unroll
;           for (int st = 1; st <= 4; ++st) { const s16x8 p0 = accfrag(Pm, 0), p1 = accfrag(Pm, 1), q0 = accfrag(Qm, 0), q1 = accfrag(Qm, 1);
;               f32x16 nP, nQ;
; #pragma unroll
;               for (int i = 0; i < 16; ++i) { nP[i] = 0.f; nQ[i] = 0.f; }
;               nP = MFMA32(q0, p0, nP); nP = MFMA32(q1, p1, nP);
;               if (st < 4) { nQ = MFMA32(p0, q0, nQ); nQ = MFMA32(p1, q1, nQ); }
;               Pm = nP; Qm = nQ;
;               const s16x8 n0 = accfrag(Pm, 0), n1 = accfrag(Pm, 1), a0 = accfrag(Aq, 0), a1 = accfrag(Aq, 1);
;               Aq = MFMA32(n0, a0, Aq); Aq = MFMA32(n1, a1, Aq); }
;           f32x4 tv; tv[0] = w == 0 ? Aq[0] : w == 1 ? Aq[4] : w == 2 ? Aq[8] : Aq[12]; tv[1] = w == 0 ? Aq[1] : w == 1 ? Aq[5] : w == 2 ? Aq[9] : Aq[13];
;           tv[2] = w == 0 ? Aq[2] : w == 1 ? Aq[6] : w == 2 ? Aq[10] : Aq[14]; tv[3] = w == 0 ? Aq[3] : w == 1 ? Aq[7] : w == 2 ? Aq[11] : Aq[15];
	v_cndmask_b32_e64 v30, 0, v14, s[82:83]
	v_cndmask_b32_e64 v33, 0, v17, s[88:89]
	v_cndmask_b32_e64 v32, 0, v16, s[90:91]
	v_cvt_pk_bf16_f32 v204, v26, v27
	v_cvt_pk_bf16_f32 v205, v28, v29
	v_cvt_pk_bf16_f32 v206, v30, v31
	v_cvt_pk_bf16_f32 v207, v32, v33
	v_pk_add_f32 v[10:11], v[112:113], v[26:27]
	v_pk_add_f32 v[12:13], v[114:115], v[28:29]
	v_pk_add_f32 v[14:15], v[116:117], v[30:31]
	v_pk_add_f32 v[16:17], v[118:119], v[32:33]
	v_mfma_f32_32x32x16_bf16 v[34:49], v[204:207], v[200:203], v[34:49]
	v_mfma_f32_32x32x16_bf16 v[18:33], v[18:21], v[22:25], 0
	v_mfma_f32_32x32x16_bf16 v[18:33], v[200:203], v[204:207], v[18:33]
	s_nop 9
	v_cvt_pk_bf16_f32 v200, v34, v35
	v_cvt_pk_bf16_f32 v201, v36, v37
	v_cvt_pk_bf16_f32 v202, v38, v39
	v_cvt_pk_bf16_f32 v203, v40, v41
	v_cvt_pk_bf16_f32 v34, v2, v3
	v_cvt_pk_bf16_f32 v35, v4, v5
	v_cvt_pk_bf16_f32 v36, v6, v7
	v_cvt_pk_bf16_f32 v37, v8, v9
	v_cvt_pk_bf16_f32 v38, v10, v11
	v_cvt_pk_bf16_f32 v39, v12, v13
	v_cvt_pk_bf16_f32 v40, v14, v15
	v_cvt_pk_bf16_f32 v41, v16, v17
	v_mfma_f32_32x32x16_bf16 v[2:17], v[200:203], v[34:37], v[2:17]
	v_cvt_pk_bf16_f32 v204, v42, v43
	v_cvt_pk_bf16_f32 v205, v44, v45
	v_cvt_pk_bf16_f32 v206, v46, v47
	v_cvt_pk_bf16_f32 v207, v48, v49
	v_cvt_pk_bf16_f32 v18, v18, v19
	v_cvt_pk_bf16_f32 v19, v20, v21
	v_cvt_pk_bf16_f32 v20, v22, v23
	v_cvt_pk_bf16_f32 v21, v24, v25
	v_mfma_f32_32x32x16_bf16 v[2:17], v[204:207], v[38:41], v[2:17]
	v_cvt_pk_bf16_f32 v208, v26, v27
	v_cvt_pk_bf16_f32 v209, v28, v29
	v_cvt_pk_bf16_f32 v210, v30, v31
	v_cvt_pk_bf16_f32 v211, v32, v33
	v_mfma_f32_32x32x16_bf16 v[34:49], v[18:21], v[200:203], 0
	s_nop 0
	v_mfma_f32_32x32x16_bf16 v[34:49], v[208:211], v[204:207], v[34:49]
	v_mfma_f32_32x32x16_bf16 v[18:33], v[200:203], v[18:21], 0
	s_nop 10
	v_cvt_pk_bf16_f32 v200, v34, v35
	v_cvt_pk_bf16_f32 v201, v36, v37
	v_cvt_pk_bf16_f32 v202, v38, v39
	v_cvt_pk_bf16_f32 v203, v40, v41
	v_cvt_pk_bf16_f32 v34, v2, v3
	v_cvt_pk_bf16_f32 v35, v4, v5
	v_cvt_pk_bf16_f32 v36, v6, v7
	v_mfma_f32_32x32x16_bf16 v[18:33], v[204:207], v[208:211], v[18:33]
	v_cvt_pk_bf16_f32 v37, v8, v9
	v_cvt_pk_bf16_f32 v38, v10, v11
	v_cvt_pk_bf16_f32 v39, v12, v13
	v_cvt_pk_bf16_f32 v40, v14, v15
	v_cvt_pk_bf16_f32 v41, v16, v17
	v_cvt_pk_bf16_f32 v204, v42, v43
	v_cvt_pk_bf16_f32 v205, v44, v45
	v_mfma_f32_32x32x16_bf16 v[2:17], v[200:203], v[34:37], v[2:17]
	v_cvt_pk_bf16_f32 v206, v46, v47
	v_cvt_pk_bf16_f32 v207, v48, v49
	s_nop 1
	v_cvt_pk_bf16_f32 v18, v18, v19
	v_cvt_pk_bf16_f32 v19, v20, v21
	v_cvt_pk_bf16_f32 v20, v22, v23
	v_cvt_pk_bf16_f32 v21, v24, v25
	v_cvt_pk_bf16_f32 v208, v26, v27
	v_mfma_f32_32x32x16_bf16 v[2:17], v[204:207], v[38:41], v[2:17]
	v_cvt_pk_bf16_f32 v209, v28, v29
	v_cvt_pk_bf16_f32 v210, v30, v31
	v_cvt_pk_bf16_f32 v211, v32, v33
	v_mfma_f32_32x32x16_bf16 v[34:49], v[18:21], v[200:203], 0
	v_mfma_f32_32x32x16_bf16 v[18:33], v[200:203], v[18:21], 0
	v_mfma_f32_32x32x16_bf16 v[34:49], v[208:211], v[204:207], v[34:49]
	v_mfma_f32_32x32x16_bf16 v[18:33], v[204:207], v[208:211], v[18:33]
	s_nop 10
	v_cvt_pk_bf16_f32 v34, v34, v35
	v_cvt_pk_bf16_f32 v35, v36, v37
	v_cvt_pk_bf16_f32 v36, v38, v39
	v_cvt_pk_bf16_f32 v37, v40, v41
	v_cvt_pk_bf16_f32 v38, v42, v43
	v_cvt_pk_bf16_f32 v39, v44, v45
	v_cvt_pk_bf16_f32 v42, v2, v3
	v_cvt_pk_bf16_f32 v18, v18, v19
	v_cvt_pk_bf16_f32 v19, v20, v21
	v_cvt_pk_bf16_f32 v20, v22, v23
	v_cvt_pk_bf16_f32 v21, v24, v25
	v_cvt_pk_bf16_f32 v43, v4, v5
	v_cvt_pk_bf16_f32 v44, v6, v7
	v_cvt_pk_bf16_f32 v45, v8, v9
	v_cvt_pk_bf16_f32 v40, v46, v47
	v_cvt_pk_bf16_f32 v41, v48, v49
	v_cvt_pk_bf16_f32 v46, v10, v11
	v_cvt_pk_bf16_f32 v47, v12, v13
	v_cvt_pk_bf16_f32 v48, v14, v15
	v_cvt_pk_bf16_f32 v49, v16, v17
	v_mfma_f32_32x32x16_bf16 v[2:17], v[34:37], v[42:45], v[2:17]
	v_cvt_pk_bf16_f32 v42, v26, v27
	v_cvt_pk_bf16_f32 v43, v28, v29
	v_cvt_pk_bf16_f32 v44, v30, v31
	v_cvt_pk_bf16_f32 v45, v32, v33
	v_mfma_f32_32x32x16_bf16 v[18:33], v[18:21], v[34:37], 0
	s_nop 0
	v_mfma_f32_32x32x16_bf16 v[18:33], v[42:45], v[38:41], v[18:33]
	v_mfma_f32_32x32x16_bf16 v[2:17], v[38:41], v[46:49], v[2:17]
	s_nop 10
	v_cvt_pk_bf16_f32 v18, v18, v19
	v_cvt_pk_bf16_f32 v19, v20, v21
	v_cvt_pk_bf16_f32 v20, v22, v23
	v_cvt_pk_bf16_f32 v21, v24, v25
	v_cvt_pk_bf16_f32 v22, v26, v27
	v_cvt_pk_bf16_f32 v23, v28, v29
	v_cvt_pk_bf16_f32 v24, v30, v31
	v_cvt_pk_bf16_f32 v26, v2, v3
	v_cvt_pk_bf16_f32 v27, v4, v5
	v_cvt_pk_bf16_f32 v28, v6, v7
	v_cvt_pk_bf16_f32 v29, v8, v9
	v_cvt_pk_bf16_f32 v25, v32, v33
	v_cvt_pk_bf16_f32 v30, v10, v11
	v_cvt_pk_bf16_f32 v31, v12, v13
	v_cvt_pk_bf16_f32 v32, v14, v15
	v_cvt_pk_bf16_f32 v33, v16, v17
	v_mfma_f32_32x32x16_bf16 v[2:17], v[18:21], v[26:29], v[2:17]
	s_nop 0
	v_mfma_f32_32x32x16_bf16 v[2:17], v[22:25], v[30:33], v[2:17]
	s_cbranch_vccnz .LBB0_1025
	s_and_b64 vcc, exec, s[2:3]
	s_cbranch_vccnz .LBB0_1028

; #define LAS __attribute__((address_space(3)))
; __device__ __forceinline__ unsigned long long pack4bf(f32x4 v) { return (unsigned long long)pk2(v[0], v[1]) | ((unsigned long long)pk2(v[2], v[3]) << 32); }
; __device__ __forceinline__ void rwkv_chunk_unit(Frame& F, int unit, LAS unsigned char* regB, LAS unsigned* bcnt, unsigned& btarget) {
;     ...
;           *(LAS unsigned long long*)(Acb + 32 * LS + tq * LS + 8 * w + 4 * hq) = pack4bf(tv); }
;         rw_bar(bcnt, btarget, lane);
;     ...
;         { f32x4 z = (f32x4){0.f, 0.f, 0.f, 0.f};
; #pragma unroll
;           for (int ks = 0; ks < 2; ++ks) { const s16x8 sb = *(const LAS s16x8*)(Sb + (16 * nj + fr) * KS + 32 * ks + 8 * fq);
;               z = __builtin_amdgcn_mfma_f32_16x16x32_bf16(*(const LAS s16x8*)(At + (16 * mi + fr) * KS + 32 * ks + 8 * fq), sb, z, 0, 0, 0);
;               yv = __builtin_amdgcn_mfma_f32_16x16x32_bf16(*(const LAS s16x8*)(Rt + (16 * mi + fr) * KS + 32 * ks + 8 * fq), sb, yv, 0, 0, 0); }
;           const s16x8 vt_ = tr_frag(Vv, LS, 8 * fq, 16 * nj, fr);
.LBB0_1037:
	s_nop 3
	v_cvt_pk_bf16_f32 v2, v2, v3
	v_cvt_pk_bf16_f32 v3, v4, v5
	ds_write_b64 v189, v[2:3] offset:40960
	ds_read_b128 v[212:215], v105 offset:20992
	ds_read_b128 v[216:219], v168
	ds_read_b128 v[220:223], v168 offset:13824
	ds_read_b128 v[224:227], v105 offset:21056
	ds_read_b128 v[228:231], v168 offset:64
	ds_read_b128 v[232:235], v168 offset:13888
	ds_read_b64_tr_b16 v[244:245], v172 offset:18432
	ds_read_b64_tr_b16 v[246:247], v172 offset:18752
	s_and_saveexec_b64 s[4:5], s[6:7]
	s_cbranch_execz .LBB0_1040
	s_mov_b64 s[10:11], exec
	v_mbcnt_lo_u32_b32 v2, s10, 0
	v_mbcnt_hi_u32_b32 v2, s11, v2
	v_cmp_eq_u32_e32 vcc, 0, v2
	s_and_b64 s[96:97], exec, vcc
	s_mov_b64 exec, s[96:97]
	s_bcnt1_i32_b64 s10, s[10:11]
	v_mov_b32_e32 v2, s12
	v_mov_b32_e32 v3, s10
	s_waitcnt lgkmcnt(8)
	ds_add_u32 v2, v3

; #define LAS __attribute__((address_space(3)))
; __device__ __forceinline__ unsigned long long pack4bf(f32x4 v) { return (unsigned long long)pk2(v[0], v[1]) | ((unsigned long long)pk2(v[2], v[3]) << 32); }
; __device__ __forceinline__ void rwkv_chunk_unit(Frame& F, int unit, LAS unsigned char* regB, LAS unsigned* bcnt, unsigned& btarget) {
;     ...
;         { f32x4 z = (f32x4){0.f, 0.f, 0.f, 0.f};
; #pragma unroll
;           for (int ks = 0; ks < 2; ++ks) { const s16x8 sb = *(const LAS s16x8*)(Sb + (16 * nj + fr) * KS + 32 * ks + 8 * fq);
;               z = __builtin_amdgcn_mfma_f32_16x16x32_bf16(*(const LAS s16x8*)(At + (16 * mi + fr) * KS + 32 * ks + 8 * fq), sb, z, 0, 0, 0);
;               yv = __builtin_amdgcn_mfma_f32_16x16x32_bf16(*(const LAS s16x8*)(Rt + (16 * mi + fr) * KS + 32 * ks + 8 * fq), sb, yv, 0, 0, 0); }
;           const s16x8 vt_ = tr_frag(Vv, LS, 8 * fq, 16 * nj, fr);
;           z = __builtin_amdgcn_mfma_f32_16x16x32_bf16(*(const LAS s16x8*)(G2b + (16 * mi + fr) * LS + 8 * fq), vt_, z, 0, 0, 0);
;           yv = __builtin_amdgcn_mfma_f32_16x16x32_bf16(*(const LAS s16x8*)(G4b + (16 * mi + fr) * LS + 8 * fq), vt_, yv, 0, 0, 0);
;           *(LAS unsigned long long*)(RHt + (16 * nj + fr) * LS + 16 * mi + 4 * fq) = pack4bf(z); }
;         rw_bar(bcnt, btarget, lane);
.LBB0_1044:
	ds_read_b128 v[10:13], v173 offset:25600
	ds_read_b128 v[14:17], v173 offset:30720
	v_mfma_f32_16x16x32_bf16 v[6:9], v[216:219], v[212:215], 0
	v_mfma_f32_16x16x32_bf16 v[2:5], v[220:223], v[212:215], 0
	v_mfma_f32_16x16x32_bf16 v[6:9], v[228:231], v[224:227], v[6:9]
	v_mfma_f32_16x16x32_bf16 v[2:5], v[232:235], v[224:227], v[2:5]
	s_waitcnt lgkmcnt(1)
	v_mfma_f32_16x16x32_bf16 v[6:9], v[10:13], v[244:247], v[6:9]
	s_waitcnt lgkmcnt(0)
	v_mfma_f32_16x16x32_bf16 v[2:5], v[14:17], v[244:247], v[2:5]
	s_nop 5
	v_cvt_pk_bf16_f32 v6, v6, v7
	v_cvt_pk_bf16_f32 v7, v8, v9
	ds_write_b64 v174, v[6:7]
	s_and_saveexec_b64 s[4:5], s[6:7]
	s_cbranch_execz .LBB0_1047
	s_mov_b64 s[10:11], exec
	v_mbcnt_lo_u32_b32 v6, s10, 0
	v_mbcnt_hi_u32_b32 v6, s11, v6
	v_cmp_eq_u32_e32 vcc, 0, v6
	s_and_b64 s[96:97], exec, vcc
	s_mov_b64 exec, s[96:97]
	s_bcnt1_i32_b64 s10, s[10:11]
	v_mov_b32_e32 v6, s12
	v_mov_b32_e32 v7, s10
	s_waitcnt lgkmcnt(0)
	ds_add_u32 v6, v7
